# P3 GLA scan: per-step state update split over waves 0,5,6,7 (two row tiles each) instead of wave 0 alone
# speedup vs baseline: 1.0027x; 1.0027x over previous
; #define LAS __attribute__((address_space(3)))
; __device__ __forceinline__ unsigned cvtpk(float lo, float hi) { f32x2 v = {lo, hi}; bf16x2_t b = __builtin_convertvector(v, bf16x2_t); return __builtin_bit_cast(unsigned, b); }
; __device__ __forceinline__ void gla_scan_chain(Frame& F, int chain) {
;     ...
;         if (wave == 0) {
;             bf16x8 vf[2]; gs_vfrag(base + GS_V, lane, vf);
;             bf16x8 kf[8][2]; f32x4 dc[8];
; #pragma unroll
;             for (int mt = 0; mt < 8; ++mt) { const int r = 16 * mt + fr; dc[mt] = *(const LAS f32x4*)(base + GS_DEC + (16 * mt + 4 * fq) * 4);
; #pragma unroll
;                 for (int ks = 0; ks < 2; ++ks) kf[mt][ks] = *(const LAS bf16x8*)(base + GS_KDT + r * 128 + (((4 * ks + fq) ^ (r & 7)) * 16)); }
;             __builtin_amdgcn_sched_barrier(0);
;             LAS unsigned char* sb = F.lds + GS_SB + ((n + 1) & 1) * GS_SBBUF + fr * GS_SBROW + 8 * fq;
; #pragma unroll
;             for (int mt = 0; mt < 8; ++mt) { f32x4 s = S[mt] * dc[mt];
;                 s = __builtin_amdgcn_mfma_f32_16x16x32_bf16(kf[mt][0], vf[0], s, 0, 0, 0); s = __builtin_amdgcn_mfma_f32_16x16x32_bf16(kf[mt][1], vf[1], s, 0, 0, 0); S[mt] = s; }
; #pragma unroll
;             for (int mt = 0; mt < 8; ++mt) { u32x2 w; w.x = cvtpk(S[mt][0], S[mt][1]); w.y = cvtpk(S[mt][2], S[mt][3]); *(LAS u32x2*)(sb + 32 * mt) = w; }
.LBB0_378:
	v_readlane_b32 s30, v254, 23
	v_add_u32_e32 v3, s34, v92
	v_add3_u32 v3, v3, v93, s51
	ds_read_b64_tr_b16 v[112:113], v3
	ds_read_b64_tr_b16 v[114:115], v3 offset:128
	ds_read_b64_tr_b16 v[108:109], v3 offset:1024
	ds_read_b64_tr_b16 v[110:111], v3 offset:1152
	s_sub_i32 s31, s30, 4
	s_max_i32 s31, s31, 0
	s_lshl_b32 s30, s31, 7
	v_add_u32_e32 v3, s34, v94
	v_add_u32_e32 v3, s30, v3
	s_lshl_b32 s30, s31, 12
	v_add_u32_e32 v4, s34, v97
	v_add_u32_e32 v4, s30, v4
	v_add_u32_e32 v5, v4, v98
	v_add_u32_e32 v4, v4, v99
	ds_read_b128 v[116:119], v3 offset:43008
	ds_read_b128 v[120:123], v3 offset:43072
	ds_read_b128 v[124:127], v5 offset:24576
	ds_read_b128 v[132:135], v5 offset:26624
	ds_read_b128 v[136:139], v4 offset:24576
	ds_read_b128 v[140:143], v4 offset:26624
	s_andn2_b32 s30, 1, s37
	s_mulk_i32 s30, 0x1100
	s_lshl_b32 s31, s31, 6
	s_add_i32 s30, s30, s31
	s_waitcnt lgkmcnt(0)
	v_pk_mul_f32 v[12:13], v[12:13], v[118:119]
	v_pk_mul_f32 v[10:11], v[10:11], v[116:117]
	v_pk_mul_f32 v[16:17], v[16:17], v[122:123]
	v_pk_mul_f32 v[14:15], v[14:15], v[120:121]
	v_add_u32_e32 v3, s30, v105
	s_nop 0
	v_mfma_f32_16x16x32_bf16 v[10:13], v[124:127], v[112:115], v[10:13]
	v_mfma_f32_16x16x32_bf16 v[14:17], v[132:135], v[112:115], v[14:17]
	v_mfma_f32_16x16x32_bf16 v[10:13], v[136:139], v[108:111], v[10:13]
	v_mfma_f32_16x16x32_bf16 v[14:17], v[140:143], v[108:111], v[14:17]
	s_nop 7
	s_nop 3
	v_cvt_pk_bf16_f32 v4, v10, v11
	v_cvt_pk_bf16_f32 v5, v12, v13
	s_nop 1
	v_cvt_pk_bf16_f32 v116, v14, v15
	v_cvt_pk_bf16_f32 v117, v16, v17
	ds_write2_b64 v3, v[4:5], v[116:117] offset1:4
	s_and_b64 vcc, exec, s[4:5]
	s_cbranch_vccnz .LBB0_360
